# baseline (speedup 1.0000x reference)
_Z13expert_kernelPKcPKfPKiPK15HIP_vector_typeIiLj4EES4_Pf:
	s_load_dwordx2 s[4:5], s[0:1], 0x18
	s_load_dwordx2 s[10:11], s[0:1], 0x10
	s_mov_b32 s3, 0
	s_lshr_b32 s8, s2, 2
	s_mov_b32 s9, s3
	s_lshl_b64 s[6:7], s[8:9], 4
	s_waitcnt lgkmcnt(0)
	s_add_u32 s4, s4, s6
	s_addc_u32 s5, s5, s7
	s_load_dwordx4 s[12:15], s[4:5], 0x0
	s_waitcnt lgkmcnt(0)
	s_mov_b32 s6, s14
	s_cmp_eq_u32 s6, 0
	s_cbranch_scc1 .LBB3_8
	v_and_b32_e32 v6, 31, v0
	s_add_i32 s6, s6, -1
	v_min_i32_e32 v1, s6, v6
	s_waitcnt lgkmcnt(0)
	v_add_u32_e32 v2, s13, v1
	v_ashrrev_i32_e32 v3, 31, v2
	v_lshl_add_u64 v[2:3], v[2:3], 2, s[10:11]
	global_load_dword v4, v[2:3], off
	s_load_dwordx4 s[4:7], s[0:1], 0x0
	s_load_dwordx2 s[10:11], s[0:1], 0x28
	v_lshrrev_b32_e32 v7, 6, v0
	s_and_b32 s9, s2, 3
	v_lshlrev_b32_e32 v8, 7, v7
	v_mov_b32_e32 v5, 0
	v_lshlrev_b32_e32 v9, 2, v6
	v_lshl_or_b32 v12, s9, 9, v8
	v_cmp_gt_u32_e32 vcc, 25, v6
	v_lshlrev_b32_e32 v8, 8, v12
	v_bfe_u32 v1, v0, 5, 1
	v_cndmask_b32_e32 v13, 0, v9, vcc
	v_mov_b32_e32 v9, v5
	v_lshlrev_b32_e32 v2, 4, v1
	v_mov_b32_e32 v3, v5
	v_accvgpr_write_b32 a63, 0
	v_accvgpr_write_b32 a62, 0
	v_accvgpr_write_b32 a61, 0
	v_accvgpr_write_b32 a60, 0
	v_accvgpr_write_b32 a59, 0
	v_accvgpr_write_b32 a58, 0
	v_accvgpr_write_b32 a57, 0
	v_accvgpr_write_b32 a56, 0
	v_accvgpr_write_b32 a55, 0
	v_accvgpr_write_b32 a54, 0
	v_accvgpr_write_b32 a53, 0
	v_accvgpr_write_b32 a52, 0
	v_accvgpr_write_b32 a51, 0
	v_accvgpr_write_b32 a50, 0
	v_accvgpr_write_b32 a49, 0
	v_accvgpr_write_b32 a48, 0
	v_accvgpr_write_b32 a47, 0
	v_accvgpr_write_b32 a46, 0
	v_accvgpr_write_b32 a45, 0
	v_accvgpr_write_b32 a44, 0
	v_accvgpr_write_b32 a43, 0
	v_accvgpr_write_b32 a42, 0
	v_accvgpr_write_b32 a41, 0
	v_accvgpr_write_b32 a40, 0
	v_accvgpr_write_b32 a39, 0
	v_accvgpr_write_b32 a38, 0
	v_accvgpr_write_b32 a37, 0
	v_accvgpr_write_b32 a36, 0
	v_accvgpr_write_b32 a35, 0
	v_accvgpr_write_b32 a34, 0
	v_accvgpr_write_b32 a33, 0
	v_accvgpr_write_b32 a32, 0
	v_accvgpr_write_b32 a31, 0
	v_accvgpr_write_b32 a30, 0
	v_accvgpr_write_b32 a29, 0
	v_accvgpr_write_b32 a28, 0
	v_accvgpr_write_b32 a27, 0
	v_accvgpr_write_b32 a26, 0
	v_accvgpr_write_b32 a25, 0
	v_accvgpr_write_b32 a24, 0
	v_accvgpr_write_b32 a23, 0
	v_accvgpr_write_b32 a22, 0
	v_accvgpr_write_b32 a21, 0
	v_accvgpr_write_b32 a20, 0
	v_accvgpr_write_b32 a19, 0
	v_accvgpr_write_b32 a18, 0
	v_accvgpr_write_b32 a17, 0
	v_accvgpr_write_b32 a16, 0
	v_accvgpr_write_b32 a15, 0
	v_accvgpr_write_b32 a14, 0
	v_accvgpr_write_b32 a13, 0
	v_accvgpr_write_b32 a12, 0
	v_accvgpr_write_b32 a11, 0
	v_accvgpr_write_b32 a10, 0
	v_accvgpr_write_b32 a9, 0
	v_accvgpr_write_b32 a8, 0
	v_accvgpr_write_b32 a7, 0
	v_accvgpr_write_b32 a6, 0
	v_accvgpr_write_b32 a5, 0
	v_accvgpr_write_b32 a4, 0
	v_accvgpr_write_b32 a3, 0
	v_accvgpr_write_b32 a2, 0
	v_accvgpr_write_b32 a1, 0
	v_accvgpr_write_b32 a0, 0
	s_waitcnt vmcnt(0)
	v_ashrrev_i32_e32 v10, 7, v4
	v_ashrrev_i32_e32 v11, 31, v10
	v_lshlrev_b64 v[10:11], 19, v[10:11]
	v_lshlrev_b32_e32 v4, 7, v4
	s_waitcnt lgkmcnt(0)
	v_lshl_add_u64 v[10:11], s[4:5], 0, v[10:11]
	v_and_b32_e32 v4, 0x3f80, v4
	v_lshl_add_u64 v[8:9], v[10:11], 0, v[8:9]
	v_lshl_add_u64 v[8:9], v[8:9], 0, v[4:5]
	v_lshl_or_b32 v4, v1, 3, v12
	v_lshl_add_u64 v[2:3], v[8:9], 0, v[2:3]
	v_mul_hi_u32_u24_e32 v9, 0x190, v4
	v_mul_u32_u24_e32 v8, 0x190, v4
	v_mov_b32_e32 v4, 0xd1c40
	v_mad_i64_i32 v[8:9], s[0:1], s12, v4, v[8:9]
	v_lshlrev_b32_e32 v4, 2, v13
	v_lshl_add_u64 v[4:5], v[8:9], 0, v[4:5]
	v_lshl_add_u64 v[4:5], s[6:7], 0, v[4:5]
	s_mov_b32 s4, 32
	s_mov_b64 s[0:1], 0
	s_movk_i32 s5, 0x1000
	s_movk_i32 s6, 0x2000
	s_mov_b32 s7, 0

_Z12final_kernelPKfPKiPK15HIP_vector_typeIiLj4EES2_S2_S0_S0_S0_S0_Pf:
	s_load_dwordx2 s[4:5], s[0:1], 0x10
	s_ashr_i32 s3, s2, 31
	s_lshl_b64 s[6:7], s[2:3], 4
	s_waitcnt lgkmcnt(0)
	s_add_u32 s4, s4, s6
	s_addc_u32 s5, s5, s7
	s_load_dwordx4 s[4:7], s[4:5], 0x0
	s_load_dwordx2 s[12:13], s[0:1], 0x8
	s_load_dwordx2 s[18:19], s[0:1], 0x0
	s_load_dwordx4 s[8:11], s[0:1], 0x20
	s_load_dwordx2 s[16:17], s[0:1], 0x30
	s_load_dwordx4 s[36:39], s[0:1], 0x38
	s_load_dwordx2 s[40:41], s[0:1], 0x48
	s_waitcnt lgkmcnt(0)
	s_cmp_eq_u32 s6, 0
	s_cbranch_scc1 .LBB4_17
	s_movk_i32 s20, 0x51f
	s_add_i32 s21, s6, -1
	s_movk_i32 s34, 0x5556
	s_movk_i32 s35, 0x64
	v_add_u32_e32 v1, 0x100, v0
	v_add_u32_e32 v2, 0x200, v0
	v_add_u32_e32 v3, 0x300, v0
	v_min_u32_e32 v3, 0x31f, v3
	v_mul_u32_u24_e32 v4, s20, v0
	v_mul_u32_u24_e32 v5, s20, v1
	v_mul_u32_u24_e32 v6, s20, v2
	v_mul_u32_u24_e32 v7, s20, v3
	v_lshrrev_b32_e32 v4, 15, v4
	v_lshrrev_b32_e32 v5, 15, v5
	v_lshrrev_b32_e32 v6, 15, v6
	v_lshrrev_b32_e32 v7, 15, v7
	v_mul_u32_u24_e32 v8, 25, v4
	v_mul_u32_u24_e32 v9, 25, v5
	v_mul_u32_u24_e32 v10, 25, v6
	v_mul_u32_u24_e32 v11, 25, v7
	v_sub_u32_e32 v8, v0, v8
	v_sub_u32_e32 v9, v1, v9
	v_sub_u32_e32 v10, v2, v10
	v_sub_u32_e32 v11, v3, v11
	v_min_u32_e32 v12, s21, v4
	v_min_u32_e32 v13, s21, v5
	v_min_u32_e32 v14, s21, v6
	v_min_u32_e32 v15, s21, v7
	v_add_lshl_u32 v12, v12, s5, 2
	v_add_lshl_u32 v13, v13, s5, 2
	v_add_lshl_u32 v14, v14, s5, 2
	v_add_lshl_u32 v15, v15, s5, 2
	v_mul_u32_u24_e32 v130, s34, v0
	v_lshrrev_b32_e32 v130, 16, v130
	v_mul_u32_u24_e32 v131, 3, v130
	v_sub_u32_e32 v131, v0, v131
	v_min_u32_e32 v132, s21, v130
	v_add_lshl_u32 v132, v132, s5, 2
	v_lshlrev_b32_e32 v133, 2, v131
	v_min_u32_e32 v134, 0x4a, v0
	v_lshlrev_b32_e32 v134, 4, v134
	s_waitcnt lgkmcnt(0)
	s_mul_i32 s22, s4, 0x4b0
	s_add_u32 s36, s36, s22
	s_addc_u32 s37, s37, 0
	s_mul_i32 s22, s4, 12
	s_add_u32 s38, s38, s22
	s_addc_u32 s39, s39, 0
	global_load_dwordx4 v[124:127], v134, s[36:37]
	global_load_dword v128, v133, s[38:39]
	global_load_dword v129, v132, s[12:13]
	global_load_dword v12, v12, s[12:13]
	global_load_dword v13, v13, s[12:13]
	global_load_dword v14, v14, s[12:13]
	global_load_dword v15, v15, s[12:13]
	s_mul_i32 s22, s2, 0xc800
	s_add_u32 s24, s18, s22
	s_addc_u32 s25, s19, 0
	s_add_u32 s26, s24, 0x3200
	s_addc_u32 s27, s25, 0
	s_add_u32 s28, s24, 0x6400
	s_addc_u32 s29, s25, 0
	s_add_u32 s30, s24, 0x9600
	s_addc_u32 s31, s25, 0
	s_mul_i32 s22, s4, 0x190
	s_add_u32 s16, s16, s22
	s_addc_u32 s17, s17, 0
	s_mul_i32 s32, s4, 0x864
	s_addk_i32 s32, 0x800
	s_movk_i32 s33, 0x190
	v_lshlrev_b32_e32 v112, 4, v0
	v_lshlrev_b32_e32 v113, 4, v1
	v_lshlrev_b32_e32 v114, 4, v2
	v_lshlrev_b32_e32 v115, 4, v3
	v_lshlrev_b32_e32 v116, 4, v8
	v_lshlrev_b32_e32 v117, 4, v9
	v_lshlrev_b32_e32 v118, 4, v10
	v_lshlrev_b32_e32 v119, 4, v11
	v_lshlrev_b32_e32 v135, 2, v0
	v_add_u32_e32 v136, 0, v135
	v_mul_u32_u24_e32 v137, s34, v136
	v_lshrrev_b32_e32 v137, 16, v137
	v_mul_u32_u24_e32 v138, 3, v137
	v_sub_u32_e32 v138, v136, v138
	v_mad_u32_u24 v138, v138, s35, v137
	v_lshlrev_b32_e32 v4, 2, v138
	v_add_u32_e32 v136, 1, v135
	v_mul_u32_u24_e32 v137, s34, v136
	v_lshrrev_b32_e32 v137, 16, v137
	v_mul_u32_u24_e32 v138, 3, v137
	v_sub_u32_e32 v138, v136, v138
	v_mad_u32_u24 v138, v138, s35, v137
	v_lshlrev_b32_e32 v5, 2, v138
	v_add_u32_e32 v136, 2, v135
	v_mul_u32_u24_e32 v137, s34, v136
	v_lshrrev_b32_e32 v137, 16, v137
	v_mul_u32_u24_e32 v138, 3, v137
	v_sub_u32_e32 v138, v136, v138
	v_mad_u32_u24 v138, v138, s35, v137
	v_lshlrev_b32_e32 v6, 2, v138
	v_add_u32_e32 v136, 3, v135
	v_mul_u32_u24_e32 v137, s34, v136
	v_lshrrev_b32_e32 v137, 16, v137
	v_mul_u32_u24_e32 v138, 3, v137
	v_sub_u32_e32 v138, v136, v138
	v_mad_u32_u24 v138, v138, s35, v137
	v_lshlrev_b32_e32 v7, 2, v138
	s_waitcnt vmcnt(0)
	v_cmp_gt_u32_e32 vcc, 0x4b, v0
	s_and_saveexec_b64 s[14:15], vcc
	ds_write_b32 v4, v124 offset:12800
	ds_write_b32 v5, v125 offset:12800
	ds_write_b32 v6, v126 offset:12800
	ds_write_b32 v7, v127 offset:12800
	s_or_b64 exec, exec, s[14:15]
	v_lshlrev_b32_e32 v12, 2, v12
	v_lshlrev_b32_e32 v13, 2, v13
	v_lshlrev_b32_e32 v14, 2, v14
	v_lshlrev_b32_e32 v15, 2, v15
	global_load_dword v12, v12, s[8:9]
	global_load_dword v13, v13, s[8:9]
	global_load_dword v14, v14, s[8:9]
	global_load_dword v15, v15, s[8:9]
	s_waitcnt vmcnt(0)
	v_add_u32_e32 v12, s32, v12
	v_add_u32_e32 v13, s32, v13
	v_add_u32_e32 v14, s32, v14
	v_add_u32_e32 v15, s32, v15
	v_mad_u32_u24 v120, v12, s33, v116
	v_mad_u32_u24 v121, v13, s33, v117
	v_mad_u32_u24 v122, v14, s33, v118
	v_mad_u32_u24 v123, v15, s33, v119
	global_load_dwordx4 v[16:19], v120, s[10:11]
	global_load_dwordx4 v[20:23], v116, s[16:17]
	global_load_dwordx4 v[24:27], v112, s[24:25]
	global_load_dwordx4 v[28:31], v112, s[26:27]
	global_load_dwordx4 v[32:35], v112, s[28:29]
	global_load_dwordx4 v[36:39], v112, s[30:31]
	global_load_dwordx4 v[40:43], v121, s[10:11]
	global_load_dwordx4 v[44:47], v117, s[16:17]
	global_load_dwordx4 v[48:51], v113, s[24:25]
	global_load_dwordx4 v[52:55], v113, s[26:27]
	global_load_dwordx4 v[56:59], v113, s[28:29]
	global_load_dwordx4 v[60:63], v113, s[30:31]
	global_load_dwordx4 v[64:67], v122, s[10:11]
	global_load_dwordx4 v[68:71], v118, s[16:17]
	global_load_dwordx4 v[72:75], v114, s[24:25]
	global_load_dwordx4 v[76:79], v114, s[26:27]
	global_load_dwordx4 v[80:83], v114, s[28:29]
	global_load_dwordx4 v[84:87], v114, s[30:31]
	global_load_dwordx4 v[88:91], v123, s[10:11]
	global_load_dwordx4 v[92:95], v119, s[16:17]
	global_load_dwordx4 v[96:99], v115, s[24:25]
	global_load_dwordx4 v[100:103], v115, s[26:27]
	global_load_dwordx4 v[104:107], v115, s[28:29]
	global_load_dwordx4 v[108:111], v115, s[30:31]
	s_waitcnt vmcnt(18)
	v_pk_add_f32 v[24:25], v[24:25], v[28:29]
	v_pk_add_f32 v[26:27], v[26:27], v[30:31]
	v_pk_add_f32 v[32:33], v[32:33], v[36:37]
	v_pk_add_f32 v[34:35], v[34:35], v[38:39]
	v_pk_add_f32 v[24:25], v[24:25], v[32:33]
	v_pk_add_f32 v[26:27], v[26:27], v[34:35]
	v_pk_add_f32 v[16:17], v[20:21], v[16:17]
	v_pk_add_f32 v[18:19], v[22:23], v[18:19]
	v_pk_add_f32 v[24:25], v[24:25], v[16:17]
	v_pk_add_f32 v[26:27], v[26:27], v[18:19]
	v_max_f32_e32 v24, 0, v24
	v_max_f32_e32 v25, 0, v25
	v_max_f32_e32 v26, 0, v26
	v_max_f32_e32 v27, 0, v27
	ds_write_b128 v112, v[24:27]
	s_waitcnt vmcnt(12)
	v_pk_add_f32 v[48:49], v[48:49], v[52:53]
	v_pk_add_f32 v[50:51], v[50:51], v[54:55]
	v_pk_add_f32 v[56:57], v[56:57], v[60:61]
	v_pk_add_f32 v[58:59], v[58:59], v[62:63]
	v_pk_add_f32 v[48:49], v[48:49], v[56:57]
	v_pk_add_f32 v[50:51], v[50:51], v[58:59]
	v_pk_add_f32 v[40:41], v[44:45], v[40:41]
	v_pk_add_f32 v[42:43], v[46:47], v[42:43]
	v_pk_add_f32 v[48:49], v[48:49], v[40:41]
	v_pk_add_f32 v[50:51], v[50:51], v[42:43]
	v_max_f32_e32 v48, 0, v48
	v_max_f32_e32 v49, 0, v49
	v_max_f32_e32 v50, 0, v50
	v_max_f32_e32 v51, 0, v51
	ds_write_b128 v113, v[48:51]
	s_waitcnt vmcnt(6)
	v_pk_add_f32 v[72:73], v[72:73], v[76:77]
	v_pk_add_f32 v[74:75], v[74:75], v[78:79]
	v_pk_add_f32 v[80:81], v[80:81], v[84:85]
	v_pk_add_f32 v[82:83], v[82:83], v[86:87]
	v_pk_add_f32 v[72:73], v[72:73], v[80:81]
	v_pk_add_f32 v[74:75], v[74:75], v[82:83]
	v_pk_add_f32 v[64:65], v[68:69], v[64:65]
	v_pk_add_f32 v[66:67], v[70:71], v[66:67]
	v_pk_add_f32 v[72:73], v[72:73], v[64:65]
	v_pk_add_f32 v[74:75], v[74:75], v[66:67]
	v_max_f32_e32 v72, 0, v72
	v_max_f32_e32 v73, 0, v73
	v_max_f32_e32 v74, 0, v74
	v_max_f32_e32 v75, 0, v75
	ds_write_b128 v114, v[72:75]
	s_waitcnt vmcnt(0)
	v_pk_add_f32 v[96:97], v[96:97], v[100:101]
	v_pk_add_f32 v[98:99], v[98:99], v[102:103]
	v_pk_add_f32 v[104:105], v[104:105], v[108:109]
	v_pk_add_f32 v[106:107], v[106:107], v[110:111]
	v_pk_add_f32 v[96:97], v[96:97], v[104:105]
	v_pk_add_f32 v[98:99], v[98:99], v[106:107]
	v_pk_add_f32 v[88:89], v[92:93], v[88:89]
	v_pk_add_f32 v[90:91], v[94:95], v[90:91]
	v_pk_add_f32 v[96:97], v[96:97], v[88:89]
	v_pk_add_f32 v[98:99], v[98:99], v[90:91]
	v_max_f32_e32 v96, 0, v96
	v_max_f32_e32 v97, 0, v97
	v_max_f32_e32 v98, 0, v98
	v_max_f32_e32 v99, 0, v99
	ds_write_b128 v115, v[96:99]
	s_mul_i32 s14, s6, 3
	v_cmp_gt_i32_e32 vcc, s14, v0
	s_waitcnt lgkmcnt(0)
	s_barrier
	s_and_saveexec_b64 s[2:3], vcc
	s_cbranch_execz .LBB4_17
	v_mul_u32_u24_e32 v4, s33, v130
	v_mul_u32_u24_e32 v5, s33, v131
	ds_read_b128 v[16:19], v4 offset:0
	ds_read_b128 v[36:39], v5 offset:12800
	ds_read_b128 v[20:23], v4 offset:16
	ds_read_b128 v[40:43], v5 offset:12816
	ds_read_b128 v[24:27], v4 offset:32
	ds_read_b128 v[44:47], v5 offset:12832
	ds_read_b128 v[28:31], v4 offset:48
	ds_read_b128 v[48:51], v5 offset:12848
	ds_read_b128 v[32:35], v4 offset:64
	ds_read_b128 v[52:55], v5 offset:12864
	ds_read_b128 v[56:59], v4 offset:80
	ds_read_b128 v[76:79], v5 offset:12880
	ds_read_b128 v[60:63], v4 offset:96
	ds_read_b128 v[80:83], v5 offset:12896
	ds_read_b128 v[64:67], v4 offset:112
	ds_read_b128 v[84:87], v5 offset:12912
	ds_read_b128 v[68:71], v4 offset:128
	ds_read_b128 v[88:91], v5 offset:12928
	ds_read_b128 v[72:75], v4 offset:144
	ds_read_b128 v[92:95], v5 offset:12944
	s_waitcnt lgkmcnt(10)
	v_fmac_f32_e32 v128, v16, v36
	v_fmac_f32_e32 v128, v17, v37
	v_fmac_f32_e32 v128, v18, v38
	v_fmac_f32_e32 v128, v19, v39
	v_fmac_f32_e32 v128, v20, v40
	v_fmac_f32_e32 v128, v21, v41
	v_fmac_f32_e32 v128, v22, v42
	v_fmac_f32_e32 v128, v23, v43
	v_fmac_f32_e32 v128, v24, v44
	v_fmac_f32_e32 v128, v25, v45
	v_fmac_f32_e32 v128, v26, v46
	v_fmac_f32_e32 v128, v27, v47
	v_fmac_f32_e32 v128, v28, v48
	v_fmac_f32_e32 v128, v29, v49
	v_fmac_f32_e32 v128, v30, v50
	v_fmac_f32_e32 v128, v31, v51
	v_fmac_f32_e32 v128, v32, v52
	v_fmac_f32_e32 v128, v33, v53
	v_fmac_f32_e32 v128, v34, v54
	v_fmac_f32_e32 v128, v35, v55
	ds_read_b128 v[16:19], v4 offset:160
	ds_read_b128 v[36:39], v5 offset:12960
	ds_read_b128 v[20:23], v4 offset:176
	ds_read_b128 v[40:43], v5 offset:12976
	ds_read_b128 v[24:27], v4 offset:192
	ds_read_b128 v[44:47], v5 offset:12992
	ds_read_b128 v[28:31], v4 offset:208
	ds_read_b128 v[48:51], v5 offset:13008
	ds_read_b128 v[32:35], v4 offset:224
	ds_read_b128 v[52:55], v5 offset:13024
	s_waitcnt lgkmcnt(10)
	v_fmac_f32_e32 v128, v56, v76
	v_fmac_f32_e32 v128, v57, v77
	v_fmac_f32_e32 v128, v58, v78
	v_fmac_f32_e32 v128, v59, v79
	v_fmac_f32_e32 v128, v60, v80
	v_fmac_f32_e32 v128, v61, v81
	v_fmac_f32_e32 v128, v62, v82
	v_fmac_f32_e32 v128, v63, v83
	v_fmac_f32_e32 v128, v64, v84
	v_fmac_f32_e32 v128, v65, v85
	v_fmac_f32_e32 v128, v66, v86
	v_fmac_f32_e32 v128, v67, v87
	v_fmac_f32_e32 v128, v68, v88
	v_fmac_f32_e32 v128, v69, v89
	v_fmac_f32_e32 v128, v70, v90
	v_fmac_f32_e32 v128, v71, v91
	v_fmac_f32_e32 v128, v72, v92
	v_fmac_f32_e32 v128, v73, v93
	v_fmac_f32_e32 v128, v74, v94
	v_fmac_f32_e32 v128, v75, v95
	ds_read_b128 v[56:59], v4 offset:240
	ds_read_b128 v[76:79], v5 offset:13040
	ds_read_b128 v[60:63], v4 offset:256
	ds_read_b128 v[80:83], v5 offset:13056
	ds_read_b128 v[64:67], v4 offset:272
	ds_read_b128 v[84:87], v5 offset:13072
	ds_read_b128 v[68:71], v4 offset:288
	ds_read_b128 v[88:91], v5 offset:13088
	ds_read_b128 v[72:75], v4 offset:304
	ds_read_b128 v[92:95], v5 offset:13104
	s_waitcnt lgkmcnt(10)
	v_fmac_f32_e32 v128, v16, v36
	v_fmac_f32_e32 v128, v17, v37
	v_fmac_f32_e32 v128, v18, v38
	v_fmac_f32_e32 v128, v19, v39
	v_fmac_f32_e32 v128, v20, v40
	v_fmac_f32_e32 v128, v21, v41
	v_fmac_f32_e32 v128, v22, v42
	v_fmac_f32_e32 v128, v23, v43
	v_fmac_f32_e32 v128, v24, v44
	v_fmac_f32_e32 v128, v25, v45
	v_fmac_f32_e32 v128, v26, v46
	v_fmac_f32_e32 v128, v27, v47
	v_fmac_f32_e32 v128, v28, v48
	v_fmac_f32_e32 v128, v29, v49
	v_fmac_f32_e32 v128, v30, v50
	v_fmac_f32_e32 v128, v31, v51
	v_fmac_f32_e32 v128, v32, v52
	v_fmac_f32_e32 v128, v33, v53
	v_fmac_f32_e32 v128, v34, v54
	v_fmac_f32_e32 v128, v35, v55
	ds_read_b128 v[16:19], v4 offset:320
	ds_read_b128 v[36:39], v5 offset:13120
	ds_read_b128 v[20:23], v4 offset:336
	ds_read_b128 v[40:43], v5 offset:13136
	ds_read_b128 v[24:27], v4 offset:352
	ds_read_b128 v[44:47], v5 offset:13152
	ds_read_b128 v[28:31], v4 offset:368
	ds_read_b128 v[48:51], v5 offset:13168
	ds_read_b128 v[32:35], v4 offset:384
	ds_read_b128 v[52:55], v5 offset:13184
	s_waitcnt lgkmcnt(10)
	v_fmac_f32_e32 v128, v56, v76
	v_fmac_f32_e32 v128, v57, v77
	v_fmac_f32_e32 v128, v58, v78
	v_fmac_f32_e32 v128, v59, v79
	v_fmac_f32_e32 v128, v60, v80
	v_fmac_f32_e32 v128, v61, v81
	v_fmac_f32_e32 v128, v62, v82
	v_fmac_f32_e32 v128, v63, v83
	v_fmac_f32_e32 v128, v64, v84
	v_fmac_f32_e32 v128, v65, v85
	v_fmac_f32_e32 v128, v66, v86
	v_fmac_f32_e32 v128, v67, v87
	v_fmac_f32_e32 v128, v68, v88
	v_fmac_f32_e32 v128, v69, v89
	v_fmac_f32_e32 v128, v70, v90
	v_fmac_f32_e32 v128, v71, v91
	v_fmac_f32_e32 v128, v72, v92
	v_fmac_f32_e32 v128, v73, v93
	v_fmac_f32_e32 v128, v74, v94
	v_fmac_f32_e32 v128, v75, v95
	s_waitcnt lgkmcnt(0)
	v_fmac_f32_e32 v128, v16, v36
	v_fmac_f32_e32 v128, v17, v37
	v_fmac_f32_e32 v128, v18, v38
	v_fmac_f32_e32 v128, v19, v39
	v_fmac_f32_e32 v128, v20, v40
	v_fmac_f32_e32 v128, v21, v41
	v_fmac_f32_e32 v128, v22, v42
	v_fmac_f32_e32 v128, v23, v43
	v_fmac_f32_e32 v128, v24, v44
	v_fmac_f32_e32 v128, v25, v45
	v_fmac_f32_e32 v128, v26, v46
	v_fmac_f32_e32 v128, v27, v47
	v_fmac_f32_e32 v128, v28, v48
	v_fmac_f32_e32 v128, v29, v49
	v_fmac_f32_e32 v128, v30, v50
	v_fmac_f32_e32 v128, v31, v51
	v_fmac_f32_e32 v128, v32, v52
	v_fmac_f32_e32 v128, v33, v53
	v_fmac_f32_e32 v128, v34, v54
	v_fmac_f32_e32 v128, v35, v55
	v_mul_u32_u24_e32 v6, 3, v129
	v_add_lshl_u32 v6, v6, v131, 2
	global_store_dword v6, v128, s[40:41]
